# speedup vs baseline: 1.0402x; 1.0402x over previous
_Z11gram_kernelPKfPKiS0_S0_S0_S0_S0_S0_S0_S0_S0_Pf:
	s_load_dwordx4 s[24:27], s[0:1], 0x0
	s_load_dwordx2 s[28:29], s[0:1], 0x40
	s_load_dwordx4 s[20:23], s[0:1], 0x30
	s_load_dwordx2 s[10:11], s[0:1], 0x58
	s_load_dwordx2 s[44:45], s[0:1], 0x20
	s_load_dwordx2 s[68:69], s[0:1], 0x10
	s_ashr_i32 s30, s2, 1
	v_mov_b32_e32 v11, 0
	s_ashr_i32 s31, s30, 31
	s_lshl_b32 s46, s30, 11
	s_lshl_b32 s3, s2, 10
	s_ashr_i32 s47, s46, 31
	s_and_b32 s33, s3, 0x400
	v_lshlrev_b32_e32 v46, 2, v0
	v_mov_b32_e32 v47, 0
	v_lshlrev_b32_e32 v212, 1, v0
	v_mov_b32_e32 v213, v47
	v_lshrrev_b32_e32 v219, 6, v0
	v_bfe_u32 v214, v0, 5, 1
	v_and_b32_e32 v220, 31, v0
	s_or_b32 s3, s46, s33
	v_lshlrev_b32_e32 v216, 4, v219
	v_lshlrev_b32_e32 v221, 3, v214
	v_or3_b32 v1, s3, v216, v221
	v_lshlrev_b32_e32 v232, 4, v220
	v_and_b32_e32 v218, 63, v0
	s_mov_b32 s39, 0x20000
	s_brev_b32 s38, 16
	v_lshl_or_b32 v180, v1, 9, v232
	v_add_u32_e32 v1, 0x10000, v180
	s_lshl_b64 s[4:5], s[46:47], 2
	s_lshl_b32 s3, s33, 2
	s_waitcnt lgkmcnt(0)
	s_mov_b64 s[36:37], s[24:25]
	s_and_b32 s37, s37, 0xffff
	s_add_u32 s26, s26, s4
	s_addc_u32 s27, s27, s5
	s_add_u32 s26, s26, s3
	s_addc_u32 s27, s27, 0
	v_lshl_add_u64 v[32:33], v[212:213], 2, s[26:27]
	global_load_dwordx2 v[32:33], v[32:33], off
	buffer_load_dwordx4 v[34:37], v180, s[36:39], 0 offen nt
	buffer_load_dwordx4 v[38:41], v180, s[36:39], 0 offen offset:512 nt
	buffer_load_dwordx4 v[42:45], v180, s[36:39], 0 offen offset:1024 nt
	buffer_load_dwordx4 v[96:99], v180, s[36:39], 0 offen offset:1536 nt
	buffer_load_dwordx4 v[100:103], v180, s[36:39], 0 offen offset:2048 nt
	buffer_load_dwordx4 v[104:107], v180, s[36:39], 0 offen offset:2560 nt
	buffer_load_dwordx4 v[108:111], v180, s[36:39], 0 offen offset:3072 nt
	buffer_load_dwordx4 v[112:115], v180, s[36:39], 0 offen offset:3584 nt
	buffer_load_dwordx4 v[116:119], v1, s[36:39], 0 offen nt
	buffer_load_dwordx4 v[120:123], v1, s[36:39], 0 offen offset:512 nt
	buffer_load_dwordx4 v[124:127], v1, s[36:39], 0 offen offset:1024 nt
	buffer_load_dwordx4 v[128:131], v1, s[36:39], 0 offen offset:1536 nt
	buffer_load_dwordx4 v[132:135], v1, s[36:39], 0 offen offset:2048 nt
	buffer_load_dwordx4 v[136:139], v1, s[36:39], 0 offen offset:2560 nt
	buffer_load_dwordx4 v[140:143], v1, s[36:39], 0 offen offset:3072 nt
	buffer_load_dwordx4 v[144:147], v1, s[36:39], 0 offen offset:3584 nt
	v_lshlrev_b32_e32 v251, 7, v0
	global_load_dword v250, v251, s[68:69]
	global_load_dword v250, v251, s[44:45]
	s_lshl_b64 s[4:5], s[30:31], 14
	s_add_u32 s48, s20, s4
	s_addc_u32 s49, s21, s5
	s_movk_i32 s3, 0x160
	v_cmp_gt_u32_e32 vcc, s3, v0
	s_mov_b32 s3, 0x10000
	v_lshrrev_b32_e32 v227, 5, v0
	v_and_b32_e32 v228, 0x7c, v46
	v_add_u32_e32 v2, 0x200, v0
	v_lshrrev_b32_e32 v229, 5, v2
	v_mul_u32_u24_e32 v246, 0x110, v227
	v_lshl_add_u32 v246, v220, 3, v246
	v_add_u32_e32 v246, 0x10000, v246
	v_lshlrev_b32_e32 v247, 2, v46
	s_waitcnt vmcnt(16)
	v_cmp_ne_u32_e64 s[6:7], 0, v32
	v_cmp_ne_u32_e64 s[4:5], 0, v33
	v_cmp_eq_u32_e64 s[8:9], 0, v218
	s_nop 0
	s_and_saveexec_b64 s[12:13], s[8:9]
	s_cbranch_execz .LBB0_6
	s_bcnt1_i32_b64 s6, s[6:7]
	s_bcnt1_i32_b64 s4, s[4:5]
	v_mov_b32_e32 v1, 0x21100
	s_add_i32 s4, s4, s6
	v_lshl_add_u32 v1, v219, 2, v1
	v_mov_b32_e32 v2, s4
	ds_write_b32 v1, v2
